# final RMSNorm rewrite with nt on the f32 output stores
# speedup vs baseline: 1.0067x; 1.0067x over previous
.LBB0_3638:
	s_or_b64 exec, exec, s[6:7]
	s_lshr_b32 s1, s97, 3
	s_mul_i32 s1, s1, s64
	v_readlane_b32 s3, v254, 12
	s_and_b32 s0, s97, 7
	s_add_i32 s1, s1, s3
	s_cmp_eq_u32 s0, 0
	s_cselect_b32 s0, s1, s2
	s_waitcnt lgkmcnt(0)
	s_barrier
	s_lshl_b32 s1, s0, 3
	s_nop 0
	v_readfirstlane_b32 s0, v0
	s_lshl_b32 s13, s97, 3
	s_ashr_i32 s2, s0, 6
	s_add_i32 s12, s2, s1
	s_cmp_lt_i32 s12, 0x10000
	s_cbranch_scc0 .LBB0_3641
	s_load_dwordx4 s[4:7], s[90:91], 0xc0
	s_load_dwordx2 s[8:9], s[90:91], 0x28
	v_and_b32_e32 v1, 63, v0
	v_lshlrev_b32_e32 v2, 4, v1
	v_lshlrev_b32_e32 v3, 3, v1
	v_and_b32_e32 v4, 15, v1
	v_lshlrev_b32_e32 v4, 18, v4
	v_mov_b32_e32 v5, 0x358637bd
	s_lshl_b32 s20, s13, 2
	s_lshl_b32 s21, s13, 11
	s_lshl_b32 s22, s13, 12
	s_mul_i32 s23, s13, 7
	s_waitcnt lgkmcnt(0)
	global_load_dwordx4 v[8:11], v2, s[8:9] offset:0
	global_load_dwordx4 v[12:15], v2, s[8:9] offset:1024
	global_load_dwordx4 v[16:19], v2, s[8:9] offset:2048
	global_load_dwordx4 v[20:23], v2, s[8:9] offset:3072
	s_ashr_i32 s15, s12, 31
	s_mov_b32 s14, s12
	s_lshl_b64 s[16:17], s[14:15], 2
	s_add_u32 s16, s16, 0x72000000
	s_addc_u32 s17, s17, 0
	s_add_u32 s16, s16, s6
	s_addc_u32 s17, s17, s7
	s_lshl_b64 s[18:19], s[14:15], 11
	s_add_u32 s18, s18, 0x26c00000
	s_addc_u32 s19, s19, 0
	s_add_u32 s18, s18, s6
	s_addc_u32 s19, s19, s7
	s_lshl_b64 s[24:25], s[14:15], 12
	s_add_u32 s24, s24, s4
	s_addc_u32 s25, s25, s5
	s_add_i32 s14, s12, s23
	s_cmp_lt_i32 s14, 0x10000
	s_cbranch_scc0 .Lfin_tail
	s_mov_b64 s[26:27], s[16:17]
	s_mov_b64 s[28:29], s[18:19]
	global_load_dword v40, v4, s[26:27]
	global_load_dwordx2 v[32:33], v3, s[28:29] offset:0
	global_load_dwordx2 v[34:35], v3, s[28:29] offset:512
	global_load_dwordx2 v[36:37], v3, s[28:29] offset:1024
	global_load_dwordx2 v[38:39], v3, s[28:29] offset:1536
	s_add_u32 s16, s16, s20
	s_addc_u32 s17, s17, 0
	s_add_u32 s18, s18, s21
	s_addc_u32 s19, s19, 0
	s_add_i32 s12, s12, s13
	s_mov_b64 s[30:31], s[16:17]
	s_mov_b64 s[32:33], s[18:19]
	global_load_dword v50, v4, s[30:31]
	global_load_dwordx2 v[42:43], v3, s[32:33] offset:0
	global_load_dwordx2 v[44:45], v3, s[32:33] offset:512
	global_load_dwordx2 v[46:47], v3, s[32:33] offset:1024
	global_load_dwordx2 v[48:49], v3, s[32:33] offset:1536
	s_add_u32 s16, s16, s20
	s_addc_u32 s17, s17, 0
	s_add_u32 s18, s18, s21
	s_addc_u32 s19, s19, 0
	s_add_i32 s12, s12, s13
	s_mov_b64 s[26:27], s[16:17]
	s_mov_b64 s[28:29], s[18:19]
	global_load_dword v60, v4, s[26:27]
	global_load_dwordx2 v[52:53], v3, s[28:29] offset:0
	global_load_dwordx2 v[54:55], v3, s[28:29] offset:512
	global_load_dwordx2 v[56:57], v3, s[28:29] offset:1024
	global_load_dwordx2 v[58:59], v3, s[28:29] offset:1536
	s_add_u32 s16, s16, s20
	s_addc_u32 s17, s17, 0
	s_add_u32 s18, s18, s21
	s_addc_u32 s19, s19, 0
	s_add_i32 s12, s12, s13
	s_mov_b64 s[30:31], s[16:17]
	s_mov_b64 s[32:33], s[18:19]
	global_load_dword v70, v4, s[30:31]
	global_load_dwordx2 v[62:63], v3, s[32:33] offset:0
	global_load_dwordx2 v[64:65], v3, s[32:33] offset:512
	global_load_dwordx2 v[66:67], v3, s[32:33] offset:1024
	global_load_dwordx2 v[68:69], v3, s[32:33] offset:1536
	s_add_u32 s16, s16, s20
	s_addc_u32 s17, s17, 0
	s_add_u32 s18, s18, s21
	s_addc_u32 s19, s19, 0
	s_add_i32 s12, s12, s13
	s_mov_b64 s[26:27], s[16:17]
	s_mov_b64 s[28:29], s[18:19]
	global_load_dword v80, v4, s[26:27]
	global_load_dwordx2 v[72:73], v3, s[28:29] offset:0
	global_load_dwordx2 v[74:75], v3, s[28:29] offset:512
	global_load_dwordx2 v[76:77], v3, s[28:29] offset:1024
	global_load_dwordx2 v[78:79], v3, s[28:29] offset:1536
	s_add_u32 s16, s16, s20
	s_addc_u32 s17, s17, 0
	s_add_u32 s18, s18, s21
	s_addc_u32 s19, s19, 0
	s_add_i32 s12, s12, s13
	s_mov_b64 s[30:31], s[16:17]
	s_mov_b64 s[32:33], s[18:19]
	global_load_dword v90, v4, s[30:31]
	global_load_dwordx2 v[82:83], v3, s[32:33] offset:0
	global_load_dwordx2 v[84:85], v3, s[32:33] offset:512
	global_load_dwordx2 v[86:87], v3, s[32:33] offset:1024
	global_load_dwordx2 v[88:89], v3, s[32:33] offset:1536
	s_add_u32 s16, s16, s20
	s_addc_u32 s17, s17, 0
	s_add_u32 s18, s18, s21
	s_addc_u32 s19, s19, 0
	s_add_i32 s12, s12, s13
	s_mov_b64 s[26:27], s[16:17]
	s_mov_b64 s[28:29], s[18:19]
	global_load_dword v100, v4, s[26:27]
	global_load_dwordx2 v[92:93], v3, s[28:29] offset:0
	global_load_dwordx2 v[94:95], v3, s[28:29] offset:512
	global_load_dwordx2 v[96:97], v3, s[28:29] offset:1024
	global_load_dwordx2 v[98:99], v3, s[28:29] offset:1536
	s_add_u32 s16, s16, s20
	s_addc_u32 s17, s17, 0
	s_add_u32 s18, s18, s21
	s_addc_u32 s19, s19, 0
	s_add_i32 s12, s12, s13
	s_mov_b64 s[30:31], s[16:17]
	s_mov_b64 s[32:33], s[18:19]
	global_load_dword v110, v4, s[30:31]
	global_load_dwordx2 v[102:103], v3, s[32:33] offset:0
	global_load_dwordx2 v[104:105], v3, s[32:33] offset:512
	global_load_dwordx2 v[106:107], v3, s[32:33] offset:1024
	global_load_dwordx2 v[108:109], v3, s[32:33] offset:1536
	s_add_u32 s16, s16, s20
	s_addc_u32 s17, s17, 0
	s_add_u32 s18, s18, s21
	s_addc_u32 s19, s19, 0
	s_add_i32 s12, s12, s13
	s_waitcnt vmcnt(35)
	v_add_f32_dpp v112, v40, v40 quad_perm:[1,0,3,2] row_mask:0xf bank_mask:0xf
	s_mov_b64 s[34:35], s[24:25]
	s_add_u32 s24, s24, s22
	v_add_f32_dpp v112, v112, v112 quad_perm:[2,3,0,1] row_mask:0xf bank_mask:0xf
	s_addc_u32 s25, s25, 0
	s_nop 0
	v_add_f32_dpp v112, v112, v112 row_half_mirror row_mask:0xf bank_mask:0xf
	s_nop 1
	v_add_f32_dpp v112, v112, v112 row_mirror row_mask:0xf bank_mask:0xf
	v_fmamk_f32 v112, v112, 0x3a800000, v5
	v_rsq_f32_e32 v114, v112
	v_lshlrev_b32_e32 v116, 16, v32
	v_and_b32_e32 v117, 0xffff0000, v32
	v_lshlrev_b32_e32 v118, 16, v33
	v_and_b32_e32 v119, 0xffff0000, v33
	v_lshlrev_b32_e32 v120, 16, v34
	v_and_b32_e32 v121, 0xffff0000, v34
	v_lshlrev_b32_e32 v122, 16, v35
	v_and_b32_e32 v123, 0xffff0000, v35
	v_lshlrev_b32_e32 v124, 16, v36
	v_and_b32_e32 v125, 0xffff0000, v36
	v_lshlrev_b32_e32 v126, 16, v37
	v_and_b32_e32 v127, 0xffff0000, v37
	v_lshlrev_b32_e32 v128, 16, v38
	v_and_b32_e32 v129, 0xffff0000, v38
	v_lshlrev_b32_e32 v130, 16, v39
	v_and_b32_e32 v131, 0xffff0000, v39
	v_pk_mul_f32 v[116:117], v[114:115], v[116:117] op_sel_hi:[0,1]
	v_pk_mul_f32 v[118:119], v[114:115], v[118:119] op_sel_hi:[0,1]
	v_pk_mul_f32 v[120:121], v[114:115], v[120:121] op_sel_hi:[0,1]
	v_pk_mul_f32 v[122:123], v[114:115], v[122:123] op_sel_hi:[0,1]
	v_pk_mul_f32 v[124:125], v[114:115], v[124:125] op_sel_hi:[0,1]
	v_pk_mul_f32 v[126:127], v[114:115], v[126:127] op_sel_hi:[0,1]
	v_pk_mul_f32 v[128:129], v[114:115], v[128:129] op_sel_hi:[0,1]
	v_pk_mul_f32 v[130:131], v[114:115], v[130:131] op_sel_hi:[0,1]
	v_pk_mul_f32 v[132:133], v[8:9], v[116:117]
	v_pk_mul_f32 v[134:135], v[10:11], v[118:119]
	v_pk_mul_f32 v[136:137], v[12:13], v[120:121]
	v_pk_mul_f32 v[138:139], v[14:15], v[122:123]
	v_pk_mul_f32 v[140:141], v[16:17], v[124:125]
	v_pk_mul_f32 v[142:143], v[18:19], v[126:127]
	v_pk_mul_f32 v[144:145], v[20:21], v[128:129]
	v_pk_mul_f32 v[146:147], v[22:23], v[130:131]
	global_store_dwordx4 v2, v[132:135], s[34:35] offset:0 nt
	global_store_dwordx4 v2, v[136:139], s[34:35] offset:1024 nt
	global_store_dwordx4 v2, v[140:143], s[34:35] offset:2048 nt
	global_store_dwordx4 v2, v[144:147], s[34:35] offset:3072 nt
	s_waitcnt vmcnt(34)
	v_add_f32_dpp v112, v50, v50 quad_perm:[1,0,3,2] row_mask:0xf bank_mask:0xf
	s_mov_b64 s[36:37], s[24:25]
	s_add_u32 s24, s24, s22
	v_add_f32_dpp v112, v112, v112 quad_perm:[2,3,0,1] row_mask:0xf bank_mask:0xf
	s_addc_u32 s25, s25, 0
	s_nop 0
	v_add_f32_dpp v112, v112, v112 row_half_mirror row_mask:0xf bank_mask:0xf
	s_nop 1
	v_add_f32_dpp v112, v112, v112 row_mirror row_mask:0xf bank_mask:0xf
	v_fmamk_f32 v112, v112, 0x3a800000, v5
	v_rsq_f32_e32 v114, v112
	v_lshlrev_b32_e32 v116, 16, v42
	v_and_b32_e32 v117, 0xffff0000, v42
	v_lshlrev_b32_e32 v118, 16, v43
	v_and_b32_e32 v119, 0xffff0000, v43
	v_lshlrev_b32_e32 v120, 16, v44
	v_and_b32_e32 v121, 0xffff0000, v44
	v_lshlrev_b32_e32 v122, 16, v45
	v_and_b32_e32 v123, 0xffff0000, v45
	v_lshlrev_b32_e32 v124, 16, v46
	v_and_b32_e32 v125, 0xffff0000, v46
	v_lshlrev_b32_e32 v126, 16, v47
	v_and_b32_e32 v127, 0xffff0000, v47
	v_lshlrev_b32_e32 v128, 16, v48
	v_and_b32_e32 v129, 0xffff0000, v48
	v_lshlrev_b32_e32 v130, 16, v49
	v_and_b32_e32 v131, 0xffff0000, v49
	v_pk_mul_f32 v[116:117], v[114:115], v[116:117] op_sel_hi:[0,1]
	v_pk_mul_f32 v[118:119], v[114:115], v[118:119] op_sel_hi:[0,1]
	v_pk_mul_f32 v[120:121], v[114:115], v[120:121] op_sel_hi:[0,1]
	v_pk_mul_f32 v[122:123], v[114:115], v[122:123] op_sel_hi:[0,1]
	v_pk_mul_f32 v[124:125], v[114:115], v[124:125] op_sel_hi:[0,1]
	v_pk_mul_f32 v[126:127], v[114:115], v[126:127] op_sel_hi:[0,1]
	v_pk_mul_f32 v[128:129], v[114:115], v[128:129] op_sel_hi:[0,1]
	v_pk_mul_f32 v[130:131], v[114:115], v[130:131] op_sel_hi:[0,1]
	v_pk_mul_f32 v[132:133], v[8:9], v[116:117]
	v_pk_mul_f32 v[134:135], v[10:11], v[118:119]
	v_pk_mul_f32 v[136:137], v[12:13], v[120:121]
	v_pk_mul_f32 v[138:139], v[14:15], v[122:123]
	v_pk_mul_f32 v[140:141], v[16:17], v[124:125]
	v_pk_mul_f32 v[142:143], v[18:19], v[126:127]
	v_pk_mul_f32 v[144:145], v[20:21], v[128:129]
	v_pk_mul_f32 v[146:147], v[22:23], v[130:131]
	global_store_dwordx4 v2, v[132:135], s[36:37] offset:0 nt
	global_store_dwordx4 v2, v[136:139], s[36:37] offset:1024 nt
	global_store_dwordx4 v2, v[140:143], s[36:37] offset:2048 nt
	global_store_dwordx4 v2, v[144:147], s[36:37] offset:3072 nt
	s_waitcnt vmcnt(33)
	v_add_f32_dpp v112, v60, v60 quad_perm:[1,0,3,2] row_mask:0xf bank_mask:0xf
	s_mov_b64 s[34:35], s[24:25]
	s_add_u32 s24, s24, s22
	v_add_f32_dpp v112, v112, v112 quad_perm:[2,3,0,1] row_mask:0xf bank_mask:0xf
	s_addc_u32 s25, s25, 0
	s_nop 0
	v_add_f32_dpp v112, v112, v112 row_half_mirror row_mask:0xf bank_mask:0xf
	s_nop 1
	v_add_f32_dpp v112, v112, v112 row_mirror row_mask:0xf bank_mask:0xf
	v_fmamk_f32 v112, v112, 0x3a800000, v5
	v_rsq_f32_e32 v114, v112
	v_lshlrev_b32_e32 v116, 16, v52
	v_and_b32_e32 v117, 0xffff0000, v52
	v_lshlrev_b32_e32 v118, 16, v53
	v_and_b32_e32 v119, 0xffff0000, v53
	v_lshlrev_b32_e32 v120, 16, v54
	v_and_b32_e32 v121, 0xffff0000, v54
	v_lshlrev_b32_e32 v122, 16, v55
	v_and_b32_e32 v123, 0xffff0000, v55
	v_lshlrev_b32_e32 v124, 16, v56
	v_and_b32_e32 v125, 0xffff0000, v56
	v_lshlrev_b32_e32 v126, 16, v57
	v_and_b32_e32 v127, 0xffff0000, v57
	v_lshlrev_b32_e32 v128, 16, v58
	v_and_b32_e32 v129, 0xffff0000, v58
	v_lshlrev_b32_e32 v130, 16, v59
	v_and_b32_e32 v131, 0xffff0000, v59
	v_pk_mul_f32 v[116:117], v[114:115], v[116:117] op_sel_hi:[0,1]
	v_pk_mul_f32 v[118:119], v[114:115], v[118:119] op_sel_hi:[0,1]
	v_pk_mul_f32 v[120:121], v[114:115], v[120:121] op_sel_hi:[0,1]
	v_pk_mul_f32 v[122:123], v[114:115], v[122:123] op_sel_hi:[0,1]
	v_pk_mul_f32 v[124:125], v[114:115], v[124:125] op_sel_hi:[0,1]
	v_pk_mul_f32 v[126:127], v[114:115], v[126:127] op_sel_hi:[0,1]
	v_pk_mul_f32 v[128:129], v[114:115], v[128:129] op_sel_hi:[0,1]
	v_pk_mul_f32 v[130:131], v[114:115], v[130:131] op_sel_hi:[0,1]
	v_pk_mul_f32 v[132:133], v[8:9], v[116:117]
	v_pk_mul_f32 v[134:135], v[10:11], v[118:119]
	v_pk_mul_f32 v[136:137], v[12:13], v[120:121]
	v_pk_mul_f32 v[138:139], v[14:15], v[122:123]
	v_pk_mul_f32 v[140:141], v[16:17], v[124:125]
	v_pk_mul_f32 v[142:143], v[18:19], v[126:127]
	v_pk_mul_f32 v[144:145], v[20:21], v[128:129]
	v_pk_mul_f32 v[146:147], v[22:23], v[130:131]
	global_store_dwordx4 v2, v[132:135], s[34:35] offset:0 nt
	global_store_dwordx4 v2, v[136:139], s[34:35] offset:1024 nt
	global_store_dwordx4 v2, v[140:143], s[34:35] offset:2048 nt
	global_store_dwordx4 v2, v[144:147], s[34:35] offset:3072 nt
	s_waitcnt vmcnt(32)
	v_add_f32_dpp v112, v70, v70 quad_perm:[1,0,3,2] row_mask:0xf bank_mask:0xf
	s_mov_b64 s[36:37], s[24:25]
	s_add_u32 s24, s24, s22
	v_add_f32_dpp v112, v112, v112 quad_perm:[2,3,0,1] row_mask:0xf bank_mask:0xf
	s_addc_u32 s25, s25, 0
	s_nop 0
	v_add_f32_dpp v112, v112, v112 row_half_mirror row_mask:0xf bank_mask:0xf
	s_nop 1
	v_add_f32_dpp v112, v112, v112 row_mirror row_mask:0xf bank_mask:0xf
	v_fmamk_f32 v112, v112, 0x3a800000, v5
	v_rsq_f32_e32 v114, v112
	v_lshlrev_b32_e32 v116, 16, v62
	v_and_b32_e32 v117, 0xffff0000, v62
	v_lshlrev_b32_e32 v118, 16, v63
	v_and_b32_e32 v119, 0xffff0000, v63
	v_lshlrev_b32_e32 v120, 16, v64
	v_and_b32_e32 v121, 0xffff0000, v64
	v_lshlrev_b32_e32 v122, 16, v65
	v_and_b32_e32 v123, 0xffff0000, v65
	v_lshlrev_b32_e32 v124, 16, v66
	v_and_b32_e32 v125, 0xffff0000, v66
	v_lshlrev_b32_e32 v126, 16, v67
	v_and_b32_e32 v127, 0xffff0000, v67
	v_lshlrev_b32_e32 v128, 16, v68
	v_and_b32_e32 v129, 0xffff0000, v68
	v_lshlrev_b32_e32 v130, 16, v69
	v_and_b32_e32 v131, 0xffff0000, v69
	v_pk_mul_f32 v[116:117], v[114:115], v[116:117] op_sel_hi:[0,1]
	v_pk_mul_f32 v[118:119], v[114:115], v[118:119] op_sel_hi:[0,1]
	v_pk_mul_f32 v[120:121], v[114:115], v[120:121] op_sel_hi:[0,1]
	v_pk_mul_f32 v[122:123], v[114:115], v[122:123] op_sel_hi:[0,1]
	v_pk_mul_f32 v[124:125], v[114:115], v[124:125] op_sel_hi:[0,1]
	v_pk_mul_f32 v[126:127], v[114:115], v[126:127] op_sel_hi:[0,1]
	v_pk_mul_f32 v[128:129], v[114:115], v[128:129] op_sel_hi:[0,1]
	v_pk_mul_f32 v[130:131], v[114:115], v[130:131] op_sel_hi:[0,1]
	v_pk_mul_f32 v[132:133], v[8:9], v[116:117]
	v_pk_mul_f32 v[134:135], v[10:11], v[118:119]
	v_pk_mul_f32 v[136:137], v[12:13], v[120:121]
	v_pk_mul_f32 v[138:139], v[14:15], v[122:123]
	v_pk_mul_f32 v[140:141], v[16:17], v[124:125]
	v_pk_mul_f32 v[142:143], v[18:19], v[126:127]
	v_pk_mul_f32 v[144:145], v[20:21], v[128:129]
	v_pk_mul_f32 v[146:147], v[22:23], v[130:131]
	global_store_dwordx4 v2, v[132:135], s[36:37] offset:0 nt
	global_store_dwordx4 v2, v[136:139], s[36:37] offset:1024 nt
	global_store_dwordx4 v2, v[140:143], s[36:37] offset:2048 nt
	global_store_dwordx4 v2, v[144:147], s[36:37] offset:3072 nt
.Lfin_loop:
	s_add_i32 s14, s12, s23
	s_cmp_lt_i32 s14, 0x10000
	s_cbranch_scc0 .Lfin_drain
	s_mov_b64 s[26:27], s[16:17]
	s_mov_b64 s[28:29], s[18:19]
	global_load_dword v40, v4, s[26:27]
	global_load_dwordx2 v[32:33], v3, s[28:29] offset:0
	global_load_dwordx2 v[34:35], v3, s[28:29] offset:512
	global_load_dwordx2 v[36:37], v3, s[28:29] offset:1024
	global_load_dwordx2 v[38:39], v3, s[28:29] offset:1536
	s_add_u32 s16, s16, s20
	s_addc_u32 s17, s17, 0
	s_add_u32 s18, s18, s21
	s_addc_u32 s19, s19, 0
	s_add_i32 s12, s12, s13
	s_mov_b64 s[30:31], s[16:17]
	s_mov_b64 s[32:33], s[18:19]
	global_load_dword v50, v4, s[30:31]
	global_load_dwordx2 v[42:43], v3, s[32:33] offset:0
	global_load_dwordx2 v[44:45], v3, s[32:33] offset:512
	global_load_dwordx2 v[46:47], v3, s[32:33] offset:1024
	global_load_dwordx2 v[48:49], v3, s[32:33] offset:1536
	s_add_u32 s16, s16, s20
	s_addc_u32 s17, s17, 0
	s_add_u32 s18, s18, s21
	s_addc_u32 s19, s19, 0
	s_add_i32 s12, s12, s13
	s_mov_b64 s[26:27], s[16:17]
	s_mov_b64 s[28:29], s[18:19]
	global_load_dword v60, v4, s[26:27]
	global_load_dwordx2 v[52:53], v3, s[28:29] offset:0
	global_load_dwordx2 v[54:55], v3, s[28:29] offset:512
	global_load_dwordx2 v[56:57], v3, s[28:29] offset:1024
	global_load_dwordx2 v[58:59], v3, s[28:29] offset:1536
	s_add_u32 s16, s16, s20
	s_addc_u32 s17, s17, 0
	s_add_u32 s18, s18, s21
	s_addc_u32 s19, s19, 0
	s_add_i32 s12, s12, s13
	s_mov_b64 s[30:31], s[16:17]
	s_mov_b64 s[32:33], s[18:19]
	global_load_dword v70, v4, s[30:31]
	global_load_dwordx2 v[62:63], v3, s[32:33] offset:0
	global_load_dwordx2 v[64:65], v3, s[32:33] offset:512
	global_load_dwordx2 v[66:67], v3, s[32:33] offset:1024
	global_load_dwordx2 v[68:69], v3, s[32:33] offset:1536
	s_add_u32 s16, s16, s20
	s_addc_u32 s17, s17, 0
	s_add_u32 s18, s18, s21
	s_addc_u32 s19, s19, 0
	s_add_i32 s12, s12, s13
	s_waitcnt vmcnt(51)
	v_add_f32_dpp v112, v80, v80 quad_perm:[1,0,3,2] row_mask:0xf bank_mask:0xf
	s_mov_b64 s[34:35], s[24:25]
	s_add_u32 s24, s24, s22
	v_add_f32_dpp v112, v112, v112 quad_perm:[2,3,0,1] row_mask:0xf bank_mask:0xf
	s_addc_u32 s25, s25, 0
	s_nop 0
	v_add_f32_dpp v112, v112, v112 row_half_mirror row_mask:0xf bank_mask:0xf
	s_nop 1
	v_add_f32_dpp v112, v112, v112 row_mirror row_mask:0xf bank_mask:0xf
	v_fmamk_f32 v112, v112, 0x3a800000, v5
	v_rsq_f32_e32 v114, v112
	v_lshlrev_b32_e32 v116, 16, v72
	v_and_b32_e32 v117, 0xffff0000, v72
	v_lshlrev_b32_e32 v118, 16, v73
	v_and_b32_e32 v119, 0xffff0000, v73
	v_lshlrev_b32_e32 v120, 16, v74
	v_and_b32_e32 v121, 0xffff0000, v74
	v_lshlrev_b32_e32 v122, 16, v75
	v_and_b32_e32 v123, 0xffff0000, v75
	v_lshlrev_b32_e32 v124, 16, v76
	v_and_b32_e32 v125, 0xffff0000, v76
	v_lshlrev_b32_e32 v126, 16, v77
	v_and_b32_e32 v127, 0xffff0000, v77
	v_lshlrev_b32_e32 v128, 16, v78
	v_and_b32_e32 v129, 0xffff0000, v78
	v_lshlrev_b32_e32 v130, 16, v79
	v_and_b32_e32 v131, 0xffff0000, v79
	v_pk_mul_f32 v[116:117], v[114:115], v[116:117] op_sel_hi:[0,1]
	v_pk_mul_f32 v[118:119], v[114:115], v[118:119] op_sel_hi:[0,1]
	v_pk_mul_f32 v[120:121], v[114:115], v[120:121] op_sel_hi:[0,1]
	v_pk_mul_f32 v[122:123], v[114:115], v[122:123] op_sel_hi:[0,1]
	v_pk_mul_f32 v[124:125], v[114:115], v[124:125] op_sel_hi:[0,1]
	v_pk_mul_f32 v[126:127], v[114:115], v[126:127] op_sel_hi:[0,1]
	v_pk_mul_f32 v[128:129], v[114:115], v[128:129] op_sel_hi:[0,1]
	v_pk_mul_f32 v[130:131], v[114:115], v[130:131] op_sel_hi:[0,1]
	v_pk_mul_f32 v[132:133], v[8:9], v[116:117]
	v_pk_mul_f32 v[134:135], v[10:11], v[118:119]
	v_pk_mul_f32 v[136:137], v[12:13], v[120:121]
	v_pk_mul_f32 v[138:139], v[14:15], v[122:123]
	v_pk_mul_f32 v[140:141], v[16:17], v[124:125]
	v_pk_mul_f32 v[142:143], v[18:19], v[126:127]
	v_pk_mul_f32 v[144:145], v[20:21], v[128:129]
	v_pk_mul_f32 v[146:147], v[22:23], v[130:131]
	global_store_dwordx4 v2, v[132:135], s[34:35] offset:0 nt
	global_store_dwordx4 v2, v[136:139], s[34:35] offset:1024 nt
	global_store_dwordx4 v2, v[140:143], s[34:35] offset:2048 nt
	global_store_dwordx4 v2, v[144:147], s[34:35] offset:3072 nt
	s_waitcnt vmcnt(50)
	v_add_f32_dpp v112, v90, v90 quad_perm:[1,0,3,2] row_mask:0xf bank_mask:0xf
	s_mov_b64 s[36:37], s[24:25]
	s_add_u32 s24, s24, s22
	v_add_f32_dpp v112, v112, v112 quad_perm:[2,3,0,1] row_mask:0xf bank_mask:0xf
	s_addc_u32 s25, s25, 0
	s_nop 0
	v_add_f32_dpp v112, v112, v112 row_half_mirror row_mask:0xf bank_mask:0xf
	s_nop 1
	v_add_f32_dpp v112, v112, v112 row_mirror row_mask:0xf bank_mask:0xf
	v_fmamk_f32 v112, v112, 0x3a800000, v5
	v_rsq_f32_e32 v114, v112
	v_lshlrev_b32_e32 v116, 16, v82
	v_and_b32_e32 v117, 0xffff0000, v82
	v_lshlrev_b32_e32 v118, 16, v83
	v_and_b32_e32 v119, 0xffff0000, v83
	v_lshlrev_b32_e32 v120, 16, v84
	v_and_b32_e32 v121, 0xffff0000, v84
	v_lshlrev_b32_e32 v122, 16, v85
	v_and_b32_e32 v123, 0xffff0000, v85
	v_lshlrev_b32_e32 v124, 16, v86
	v_and_b32_e32 v125, 0xffff0000, v86
	v_lshlrev_b32_e32 v126, 16, v87
	v_and_b32_e32 v127, 0xffff0000, v87
	v_lshlrev_b32_e32 v128, 16, v88
	v_and_b32_e32 v129, 0xffff0000, v88
	v_lshlrev_b32_e32 v130, 16, v89
	v_and_b32_e32 v131, 0xffff0000, v89
	v_pk_mul_f32 v[116:117], v[114:115], v[116:117] op_sel_hi:[0,1]
	v_pk_mul_f32 v[118:119], v[114:115], v[118:119] op_sel_hi:[0,1]
	v_pk_mul_f32 v[120:121], v[114:115], v[120:121] op_sel_hi:[0,1]
	v_pk_mul_f32 v[122:123], v[114:115], v[122:123] op_sel_hi:[0,1]
	v_pk_mul_f32 v[124:125], v[114:115], v[124:125] op_sel_hi:[0,1]
	v_pk_mul_f32 v[126:127], v[114:115], v[126:127] op_sel_hi:[0,1]
	v_pk_mul_f32 v[128:129], v[114:115], v[128:129] op_sel_hi:[0,1]
	v_pk_mul_f32 v[130:131], v[114:115], v[130:131] op_sel_hi:[0,1]
	v_pk_mul_f32 v[132:133], v[8:9], v[116:117]
	v_pk_mul_f32 v[134:135], v[10:11], v[118:119]
	v_pk_mul_f32 v[136:137], v[12:13], v[120:121]
	v_pk_mul_f32 v[138:139], v[14:15], v[122:123]
	v_pk_mul_f32 v[140:141], v[16:17], v[124:125]
	v_pk_mul_f32 v[142:143], v[18:19], v[126:127]
	v_pk_mul_f32 v[144:145], v[20:21], v[128:129]
	v_pk_mul_f32 v[146:147], v[22:23], v[130:131]
	global_store_dwordx4 v2, v[132:135], s[36:37] offset:0 nt
	global_store_dwordx4 v2, v[136:139], s[36:37] offset:1024 nt
	global_store_dwordx4 v2, v[140:143], s[36:37] offset:2048 nt
	global_store_dwordx4 v2, v[144:147], s[36:37] offset:3072 nt
	s_waitcnt vmcnt(49)
	v_add_f32_dpp v112, v100, v100 quad_perm:[1,0,3,2] row_mask:0xf bank_mask:0xf
	s_mov_b64 s[34:35], s[24:25]
	s_add_u32 s24, s24, s22
	v_add_f32_dpp v112, v112, v112 quad_perm:[2,3,0,1] row_mask:0xf bank_mask:0xf
	s_addc_u32 s25, s25, 0
	s_nop 0
	v_add_f32_dpp v112, v112, v112 row_half_mirror row_mask:0xf bank_mask:0xf
	s_nop 1
	v_add_f32_dpp v112, v112, v112 row_mirror row_mask:0xf bank_mask:0xf
	v_fmamk_f32 v112, v112, 0x3a800000, v5
	v_rsq_f32_e32 v114, v112
	v_lshlrev_b32_e32 v116, 16, v92
	v_and_b32_e32 v117, 0xffff0000, v92
	v_lshlrev_b32_e32 v118, 16, v93
	v_and_b32_e32 v119, 0xffff0000, v93
	v_lshlrev_b32_e32 v120, 16, v94
	v_and_b32_e32 v121, 0xffff0000, v94
	v_lshlrev_b32_e32 v122, 16, v95
	v_and_b32_e32 v123, 0xffff0000, v95
	v_lshlrev_b32_e32 v124, 16, v96
	v_and_b32_e32 v125, 0xffff0000, v96
	v_lshlrev_b32_e32 v126, 16, v97
	v_and_b32_e32 v127, 0xffff0000, v97
	v_lshlrev_b32_e32 v128, 16, v98
	v_and_b32_e32 v129, 0xffff0000, v98
	v_lshlrev_b32_e32 v130, 16, v99
	v_and_b32_e32 v131, 0xffff0000, v99
	v_pk_mul_f32 v[116:117], v[114:115], v[116:117] op_sel_hi:[0,1]
	v_pk_mul_f32 v[118:119], v[114:115], v[118:119] op_sel_hi:[0,1]
	v_pk_mul_f32 v[120:121], v[114:115], v[120:121] op_sel_hi:[0,1]
	v_pk_mul_f32 v[122:123], v[114:115], v[122:123] op_sel_hi:[0,1]
	v_pk_mul_f32 v[124:125], v[114:115], v[124:125] op_sel_hi:[0,1]
	v_pk_mul_f32 v[126:127], v[114:115], v[126:127] op_sel_hi:[0,1]
	v_pk_mul_f32 v[128:129], v[114:115], v[128:129] op_sel_hi:[0,1]
	v_pk_mul_f32 v[130:131], v[114:115], v[130:131] op_sel_hi:[0,1]
	v_pk_mul_f32 v[132:133], v[8:9], v[116:117]
	v_pk_mul_f32 v[134:135], v[10:11], v[118:119]
	v_pk_mul_f32 v[136:137], v[12:13], v[120:121]
	v_pk_mul_f32 v[138:139], v[14:15], v[122:123]
	v_pk_mul_f32 v[140:141], v[16:17], v[124:125]
	v_pk_mul_f32 v[142:143], v[18:19], v[126:127]
	v_pk_mul_f32 v[144:145], v[20:21], v[128:129]
	v_pk_mul_f32 v[146:147], v[22:23], v[130:131]
	global_store_dwordx4 v2, v[132:135], s[34:35] offset:0 nt
	global_store_dwordx4 v2, v[136:139], s[34:35] offset:1024 nt
	global_store_dwordx4 v2, v[140:143], s[34:35] offset:2048 nt
	global_store_dwordx4 v2, v[144:147], s[34:35] offset:3072 nt
	s_waitcnt vmcnt(48)
	v_add_f32_dpp v112, v110, v110 quad_perm:[1,0,3,2] row_mask:0xf bank_mask:0xf
	s_mov_b64 s[36:37], s[24:25]
	s_add_u32 s24, s24, s22
	v_add_f32_dpp v112, v112, v112 quad_perm:[2,3,0,1] row_mask:0xf bank_mask:0xf
	s_addc_u32 s25, s25, 0
	s_nop 0
	v_add_f32_dpp v112, v112, v112 row_half_mirror row_mask:0xf bank_mask:0xf
	s_nop 1
	v_add_f32_dpp v112, v112, v112 row_mirror row_mask:0xf bank_mask:0xf
	v_fmamk_f32 v112, v112, 0x3a800000, v5
	v_rsq_f32_e32 v114, v112
	v_lshlrev_b32_e32 v116, 16, v102
	v_and_b32_e32 v117, 0xffff0000, v102
	v_lshlrev_b32_e32 v118, 16, v103
	v_and_b32_e32 v119, 0xffff0000, v103
	v_lshlrev_b32_e32 v120, 16, v104
	v_and_b32_e32 v121, 0xffff0000, v104
	v_lshlrev_b32_e32 v122, 16, v105
	v_and_b32_e32 v123, 0xffff0000, v105
	v_lshlrev_b32_e32 v124, 16, v106
	v_and_b32_e32 v125, 0xffff0000, v106
	v_lshlrev_b32_e32 v126, 16, v107
	v_and_b32_e32 v127, 0xffff0000, v107
	v_lshlrev_b32_e32 v128, 16, v108
	v_and_b32_e32 v129, 0xffff0000, v108
	v_lshlrev_b32_e32 v130, 16, v109
	v_and_b32_e32 v131, 0xffff0000, v109
	v_pk_mul_f32 v[116:117], v[114:115], v[116:117] op_sel_hi:[0,1]
	v_pk_mul_f32 v[118:119], v[114:115], v[118:119] op_sel_hi:[0,1]
	v_pk_mul_f32 v[120:121], v[114:115], v[120:121] op_sel_hi:[0,1]
	v_pk_mul_f32 v[122:123], v[114:115], v[122:123] op_sel_hi:[0,1]
	v_pk_mul_f32 v[124:125], v[114:115], v[124:125] op_sel_hi:[0,1]
	v_pk_mul_f32 v[126:127], v[114:115], v[126:127] op_sel_hi:[0,1]
	v_pk_mul_f32 v[128:129], v[114:115], v[128:129] op_sel_hi:[0,1]
	v_pk_mul_f32 v[130:131], v[114:115], v[130:131] op_sel_hi:[0,1]
	v_pk_mul_f32 v[132:133], v[8:9], v[116:117]
	v_pk_mul_f32 v[134:135], v[10:11], v[118:119]
	v_pk_mul_f32 v[136:137], v[12:13], v[120:121]
	v_pk_mul_f32 v[138:139], v[14:15], v[122:123]
	v_pk_mul_f32 v[140:141], v[16:17], v[124:125]
	v_pk_mul_f32 v[142:143], v[18:19], v[126:127]
	v_pk_mul_f32 v[144:145], v[20:21], v[128:129]
	v_pk_mul_f32 v[146:147], v[22:23], v[130:131]
	global_store_dwordx4 v2, v[132:135], s[36:37] offset:0 nt
	global_store_dwordx4 v2, v[136:139], s[36:37] offset:1024 nt
	global_store_dwordx4 v2, v[140:143], s[36:37] offset:2048 nt
	global_store_dwordx4 v2, v[144:147], s[36:37] offset:3072 nt
	s_mov_b64 s[26:27], s[16:17]
	s_mov_b64 s[28:29], s[18:19]
	global_load_dword v80, v4, s[26:27]
	global_load_dwordx2 v[72:73], v3, s[28:29] offset:0
	global_load_dwordx2 v[74:75], v3, s[28:29] offset:512
	global_load_dwordx2 v[76:77], v3, s[28:29] offset:1024
	global_load_dwordx2 v[78:79], v3, s[28:29] offset:1536
	s_add_u32 s16, s16, s20
	s_addc_u32 s17, s17, 0
	s_add_u32 s18, s18, s21
	s_addc_u32 s19, s19, 0
	s_add_i32 s12, s12, s13
	s_mov_b64 s[30:31], s[16:17]
	s_mov_b64 s[32:33], s[18:19]
	global_load_dword v90, v4, s[30:31]
	global_load_dwordx2 v[82:83], v3, s[32:33] offset:0
	global_load_dwordx2 v[84:85], v3, s[32:33] offset:512
	global_load_dwordx2 v[86:87], v3, s[32:33] offset:1024
	global_load_dwordx2 v[88:89], v3, s[32:33] offset:1536
	s_add_u32 s16, s16, s20
	s_addc_u32 s17, s17, 0
	s_add_u32 s18, s18, s21
	s_addc_u32 s19, s19, 0
	s_add_i32 s12, s12, s13
	s_mov_b64 s[26:27], s[16:17]
	s_mov_b64 s[28:29], s[18:19]
	global_load_dword v100, v4, s[26:27]
	global_load_dwordx2 v[92:93], v3, s[28:29] offset:0
	global_load_dwordx2 v[94:95], v3, s[28:29] offset:512
	global_load_dwordx2 v[96:97], v3, s[28:29] offset:1024
	global_load_dwordx2 v[98:99], v3, s[28:29] offset:1536
	s_add_u32 s16, s16, s20
	s_addc_u32 s17, s17, 0
	s_add_u32 s18, s18, s21
	s_addc_u32 s19, s19, 0
	s_add_i32 s12, s12, s13
	s_mov_b64 s[30:31], s[16:17]
	s_mov_b64 s[32:33], s[18:19]
	global_load_dword v110, v4, s[30:31]
	global_load_dwordx2 v[102:103], v3, s[32:33] offset:0
	global_load_dwordx2 v[104:105], v3, s[32:33] offset:512
	global_load_dwordx2 v[106:107], v3, s[32:33] offset:1024
	global_load_dwordx2 v[108:109], v3, s[32:33] offset:1536
	s_add_u32 s16, s16, s20
	s_addc_u32 s17, s17, 0
	s_add_u32 s18, s18, s21
	s_addc_u32 s19, s19, 0
	s_add_i32 s12, s12, s13
	s_waitcnt vmcnt(51)
	v_add_f32_dpp v112, v40, v40 quad_perm:[1,0,3,2] row_mask:0xf bank_mask:0xf
	s_mov_b64 s[34:35], s[24:25]
	s_add_u32 s24, s24, s22
	v_add_f32_dpp v112, v112, v112 quad_perm:[2,3,0,1] row_mask:0xf bank_mask:0xf
	s_addc_u32 s25, s25, 0
	s_nop 0
	v_add_f32_dpp v112, v112, v112 row_half_mirror row_mask:0xf bank_mask:0xf
	s_nop 1
	v_add_f32_dpp v112, v112, v112 row_mirror row_mask:0xf bank_mask:0xf
	v_fmamk_f32 v112, v112, 0x3a800000, v5
	v_rsq_f32_e32 v114, v112
	v_lshlrev_b32_e32 v116, 16, v32
	v_and_b32_e32 v117, 0xffff0000, v32
	v_lshlrev_b32_e32 v118, 16, v33
	v_and_b32_e32 v119, 0xffff0000, v33
	v_lshlrev_b32_e32 v120, 16, v34
	v_and_b32_e32 v121, 0xffff0000, v34
	v_lshlrev_b32_e32 v122, 16, v35
	v_and_b32_e32 v123, 0xffff0000, v35
	v_lshlrev_b32_e32 v124, 16, v36
	v_and_b32_e32 v125, 0xffff0000, v36
	v_lshlrev_b32_e32 v126, 16, v37
	v_and_b32_e32 v127, 0xffff0000, v37
	v_lshlrev_b32_e32 v128, 16, v38
	v_and_b32_e32 v129, 0xffff0000, v38
	v_lshlrev_b32_e32 v130, 16, v39
	v_and_b32_e32 v131, 0xffff0000, v39
	v_pk_mul_f32 v[116:117], v[114:115], v[116:117] op_sel_hi:[0,1]
	v_pk_mul_f32 v[118:119], v[114:115], v[118:119] op_sel_hi:[0,1]
	v_pk_mul_f32 v[120:121], v[114:115], v[120:121] op_sel_hi:[0,1]
	v_pk_mul_f32 v[122:123], v[114:115], v[122:123] op_sel_hi:[0,1]
	v_pk_mul_f32 v[124:125], v[114:115], v[124:125] op_sel_hi:[0,1]
	v_pk_mul_f32 v[126:127], v[114:115], v[126:127] op_sel_hi:[0,1]
	v_pk_mul_f32 v[128:129], v[114:115], v[128:129] op_sel_hi:[0,1]
	v_pk_mul_f32 v[130:131], v[114:115], v[130:131] op_sel_hi:[0,1]
	v_pk_mul_f32 v[132:133], v[8:9], v[116:117]
	v_pk_mul_f32 v[134:135], v[10:11], v[118:119]
	v_pk_mul_f32 v[136:137], v[12:13], v[120:121]
	v_pk_mul_f32 v[138:139], v[14:15], v[122:123]
	v_pk_mul_f32 v[140:141], v[16:17], v[124:125]
	v_pk_mul_f32 v[142:143], v[18:19], v[126:127]
	v_pk_mul_f32 v[144:145], v[20:21], v[128:129]
	v_pk_mul_f32 v[146:147], v[22:23], v[130:131]
	global_store_dwordx4 v2, v[132:135], s[34:35] offset:0 nt
	global_store_dwordx4 v2, v[136:139], s[34:35] offset:1024 nt
	global_store_dwordx4 v2, v[140:143], s[34:35] offset:2048 nt
	global_store_dwordx4 v2, v[144:147], s[34:35] offset:3072 nt
	s_waitcnt vmcnt(50)
	v_add_f32_dpp v112, v50, v50 quad_perm:[1,0,3,2] row_mask:0xf bank_mask:0xf
	s_mov_b64 s[36:37], s[24:25]
	s_add_u32 s24, s24, s22
	v_add_f32_dpp v112, v112, v112 quad_perm:[2,3,0,1] row_mask:0xf bank_mask:0xf
	s_addc_u32 s25, s25, 0
	s_nop 0
	v_add_f32_dpp v112, v112, v112 row_half_mirror row_mask:0xf bank_mask:0xf
	s_nop 1
	v_add_f32_dpp v112, v112, v112 row_mirror row_mask:0xf bank_mask:0xf
	v_fmamk_f32 v112, v112, 0x3a800000, v5
	v_rsq_f32_e32 v114, v112
	v_lshlrev_b32_e32 v116, 16, v42
	v_and_b32_e32 v117, 0xffff0000, v42
	v_lshlrev_b32_e32 v118, 16, v43
	v_and_b32_e32 v119, 0xffff0000, v43
	v_lshlrev_b32_e32 v120, 16, v44
	v_and_b32_e32 v121, 0xffff0000, v44
	v_lshlrev_b32_e32 v122, 16, v45
	v_and_b32_e32 v123, 0xffff0000, v45
	v_lshlrev_b32_e32 v124, 16, v46
	v_and_b32_e32 v125, 0xffff0000, v46
	v_lshlrev_b32_e32 v126, 16, v47
	v_and_b32_e32 v127, 0xffff0000, v47
	v_lshlrev_b32_e32 v128, 16, v48
	v_and_b32_e32 v129, 0xffff0000, v48
	v_lshlrev_b32_e32 v130, 16, v49
	v_and_b32_e32 v131, 0xffff0000, v49
	v_pk_mul_f32 v[116:117], v[114:115], v[116:117] op_sel_hi:[0,1]
	v_pk_mul_f32 v[118:119], v[114:115], v[118:119] op_sel_hi:[0,1]
	v_pk_mul_f32 v[120:121], v[114:115], v[120:121] op_sel_hi:[0,1]
	v_pk_mul_f32 v[122:123], v[114:115], v[122:123] op_sel_hi:[0,1]
	v_pk_mul_f32 v[124:125], v[114:115], v[124:125] op_sel_hi:[0,1]
	v_pk_mul_f32 v[126:127], v[114:115], v[126:127] op_sel_hi:[0,1]
	v_pk_mul_f32 v[128:129], v[114:115], v[128:129] op_sel_hi:[0,1]
	v_pk_mul_f32 v[130:131], v[114:115], v[130:131] op_sel_hi:[0,1]
	v_pk_mul_f32 v[132:133], v[8:9], v[116:117]
	v_pk_mul_f32 v[134:135], v[10:11], v[118:119]
	v_pk_mul_f32 v[136:137], v[12:13], v[120:121]
	v_pk_mul_f32 v[138:139], v[14:15], v[122:123]
	v_pk_mul_f32 v[140:141], v[16:17], v[124:125]
	v_pk_mul_f32 v[142:143], v[18:19], v[126:127]
	v_pk_mul_f32 v[144:145], v[20:21], v[128:129]
	v_pk_mul_f32 v[146:147], v[22:23], v[130:131]
	global_store_dwordx4 v2, v[132:135], s[36:37] offset:0 nt
	global_store_dwordx4 v2, v[136:139], s[36:37] offset:1024 nt
	global_store_dwordx4 v2, v[140:143], s[36:37] offset:2048 nt
	global_store_dwordx4 v2, v[144:147], s[36:37] offset:3072 nt
	s_waitcnt vmcnt(49)
	v_add_f32_dpp v112, v60, v60 quad_perm:[1,0,3,2] row_mask:0xf bank_mask:0xf
	s_mov_b64 s[34:35], s[24:25]
	s_add_u32 s24, s24, s22
	v_add_f32_dpp v112, v112, v112 quad_perm:[2,3,0,1] row_mask:0xf bank_mask:0xf
	s_addc_u32 s25, s25, 0
	s_nop 0
	v_add_f32_dpp v112, v112, v112 row_half_mirror row_mask:0xf bank_mask:0xf
	s_nop 1
	v_add_f32_dpp v112, v112, v112 row_mirror row_mask:0xf bank_mask:0xf
	v_fmamk_f32 v112, v112, 0x3a800000, v5
	v_rsq_f32_e32 v114, v112
	v_lshlrev_b32_e32 v116, 16, v52
	v_and_b32_e32 v117, 0xffff0000, v52
	v_lshlrev_b32_e32 v118, 16, v53
	v_and_b32_e32 v119, 0xffff0000, v53
	v_lshlrev_b32_e32 v120, 16, v54
	v_and_b32_e32 v121, 0xffff0000, v54
	v_lshlrev_b32_e32 v122, 16, v55
	v_and_b32_e32 v123, 0xffff0000, v55
	v_lshlrev_b32_e32 v124, 16, v56
	v_and_b32_e32 v125, 0xffff0000, v56
	v_lshlrev_b32_e32 v126, 16, v57
	v_and_b32_e32 v127, 0xffff0000, v57
	v_lshlrev_b32_e32 v128, 16, v58
	v_and_b32_e32 v129, 0xffff0000, v58
	v_lshlrev_b32_e32 v130, 16, v59
	v_and_b32_e32 v131, 0xffff0000, v59
	v_pk_mul_f32 v[116:117], v[114:115], v[116:117] op_sel_hi:[0,1]
	v_pk_mul_f32 v[118:119], v[114:115], v[118:119] op_sel_hi:[0,1]
	v_pk_mul_f32 v[120:121], v[114:115], v[120:121] op_sel_hi:[0,1]
	v_pk_mul_f32 v[122:123], v[114:115], v[122:123] op_sel_hi:[0,1]
	v_pk_mul_f32 v[124:125], v[114:115], v[124:125] op_sel_hi:[0,1]
	v_pk_mul_f32 v[126:127], v[114:115], v[126:127] op_sel_hi:[0,1]
	v_pk_mul_f32 v[128:129], v[114:115], v[128:129] op_sel_hi:[0,1]
	v_pk_mul_f32 v[130:131], v[114:115], v[130:131] op_sel_hi:[0,1]
	v_pk_mul_f32 v[132:133], v[8:9], v[116:117]
	v_pk_mul_f32 v[134:135], v[10:11], v[118:119]
	v_pk_mul_f32 v[136:137], v[12:13], v[120:121]
	v_pk_mul_f32 v[138:139], v[14:15], v[122:123]
	v_pk_mul_f32 v[140:141], v[16:17], v[124:125]
	v_pk_mul_f32 v[142:143], v[18:19], v[126:127]
	v_pk_mul_f32 v[144:145], v[20:21], v[128:129]
	v_pk_mul_f32 v[146:147], v[22:23], v[130:131]
	global_store_dwordx4 v2, v[132:135], s[34:35] offset:0 nt
	global_store_dwordx4 v2, v[136:139], s[34:35] offset:1024 nt
	global_store_dwordx4 v2, v[140:143], s[34:35] offset:2048 nt
	global_store_dwordx4 v2, v[144:147], s[34:35] offset:3072 nt
	s_waitcnt vmcnt(48)
	v_add_f32_dpp v112, v70, v70 quad_perm:[1,0,3,2] row_mask:0xf bank_mask:0xf
	s_mov_b64 s[36:37], s[24:25]
	s_add_u32 s24, s24, s22
	v_add_f32_dpp v112, v112, v112 quad_perm:[2,3,0,1] row_mask:0xf bank_mask:0xf
	s_addc_u32 s25, s25, 0
	s_nop 0
	v_add_f32_dpp v112, v112, v112 row_half_mirror row_mask:0xf bank_mask:0xf
	s_nop 1
	v_add_f32_dpp v112, v112, v112 row_mirror row_mask:0xf bank_mask:0xf
	v_fmamk_f32 v112, v112, 0x3a800000, v5
	v_rsq_f32_e32 v114, v112
	v_lshlrev_b32_e32 v116, 16, v62
	v_and_b32_e32 v117, 0xffff0000, v62
	v_lshlrev_b32_e32 v118, 16, v63
	v_and_b32_e32 v119, 0xffff0000, v63
	v_lshlrev_b32_e32 v120, 16, v64
	v_and_b32_e32 v121, 0xffff0000, v64
	v_lshlrev_b32_e32 v122, 16, v65
	v_and_b32_e32 v123, 0xffff0000, v65
	v_lshlrev_b32_e32 v124, 16, v66
	v_and_b32_e32 v125, 0xffff0000, v66
	v_lshlrev_b32_e32 v126, 16, v67
	v_and_b32_e32 v127, 0xffff0000, v67
	v_lshlrev_b32_e32 v128, 16, v68
	v_and_b32_e32 v129, 0xffff0000, v68
	v_lshlrev_b32_e32 v130, 16, v69
	v_and_b32_e32 v131, 0xffff0000, v69
	v_pk_mul_f32 v[116:117], v[114:115], v[116:117] op_sel_hi:[0,1]
	v_pk_mul_f32 v[118:119], v[114:115], v[118:119] op_sel_hi:[0,1]
	v_pk_mul_f32 v[120:121], v[114:115], v[120:121] op_sel_hi:[0,1]
	v_pk_mul_f32 v[122:123], v[114:115], v[122:123] op_sel_hi:[0,1]
	v_pk_mul_f32 v[124:125], v[114:115], v[124:125] op_sel_hi:[0,1]
	v_pk_mul_f32 v[126:127], v[114:115], v[126:127] op_sel_hi:[0,1]
	v_pk_mul_f32 v[128:129], v[114:115], v[128:129] op_sel_hi:[0,1]
	v_pk_mul_f32 v[130:131], v[114:115], v[130:131] op_sel_hi:[0,1]
	v_pk_mul_f32 v[132:133], v[8:9], v[116:117]
	v_pk_mul_f32 v[134:135], v[10:11], v[118:119]
	v_pk_mul_f32 v[136:137], v[12:13], v[120:121]
	v_pk_mul_f32 v[138:139], v[14:15], v[122:123]
	v_pk_mul_f32 v[140:141], v[16:17], v[124:125]
	v_pk_mul_f32 v[142:143], v[18:19], v[126:127]
	v_pk_mul_f32 v[144:145], v[20:21], v[128:129]
	v_pk_mul_f32 v[146:147], v[22:23], v[130:131]
	global_store_dwordx4 v2, v[132:135], s[36:37] offset:0 nt
	global_store_dwordx4 v2, v[136:139], s[36:37] offset:1024 nt
	global_store_dwordx4 v2, v[140:143], s[36:37] offset:2048 nt
	global_store_dwordx4 v2, v[144:147], s[36:37] offset:3072 nt
	s_branch .Lfin_loop
.Lfin_drain:
	s_waitcnt vmcnt(31)
	v_add_f32_dpp v112, v80, v80 quad_perm:[1,0,3,2] row_mask:0xf bank_mask:0xf
	s_mov_b64 s[34:35], s[24:25]
	s_add_u32 s24, s24, s22
	v_add_f32_dpp v112, v112, v112 quad_perm:[2,3,0,1] row_mask:0xf bank_mask:0xf
	s_addc_u32 s25, s25, 0
	s_nop 0
	v_add_f32_dpp v112, v112, v112 row_half_mirror row_mask:0xf bank_mask:0xf
	s_nop 1
	v_add_f32_dpp v112, v112, v112 row_mirror row_mask:0xf bank_mask:0xf
	v_fmamk_f32 v112, v112, 0x3a800000, v5
	v_rsq_f32_e32 v114, v112
	v_lshlrev_b32_e32 v116, 16, v72
	v_and_b32_e32 v117, 0xffff0000, v72
	v_lshlrev_b32_e32 v118, 16, v73
	v_and_b32_e32 v119, 0xffff0000, v73
	v_lshlrev_b32_e32 v120, 16, v74
	v_and_b32_e32 v121, 0xffff0000, v74
	v_lshlrev_b32_e32 v122, 16, v75
	v_and_b32_e32 v123, 0xffff0000, v75
	v_lshlrev_b32_e32 v124, 16, v76
	v_and_b32_e32 v125, 0xffff0000, v76
	v_lshlrev_b32_e32 v126, 16, v77
	v_and_b32_e32 v127, 0xffff0000, v77
	v_lshlrev_b32_e32 v128, 16, v78
	v_and_b32_e32 v129, 0xffff0000, v78
	v_lshlrev_b32_e32 v130, 16, v79
	v_and_b32_e32 v131, 0xffff0000, v79
	v_pk_mul_f32 v[116:117], v[114:115], v[116:117] op_sel_hi:[0,1]
	v_pk_mul_f32 v[118:119], v[114:115], v[118:119] op_sel_hi:[0,1]
	v_pk_mul_f32 v[120:121], v[114:115], v[120:121] op_sel_hi:[0,1]
	v_pk_mul_f32 v[122:123], v[114:115], v[122:123] op_sel_hi:[0,1]
	v_pk_mul_f32 v[124:125], v[114:115], v[124:125] op_sel_hi:[0,1]
	v_pk_mul_f32 v[126:127], v[114:115], v[126:127] op_sel_hi:[0,1]
	v_pk_mul_f32 v[128:129], v[114:115], v[128:129] op_sel_hi:[0,1]
	v_pk_mul_f32 v[130:131], v[114:115], v[130:131] op_sel_hi:[0,1]
	v_pk_mul_f32 v[132:133], v[8:9], v[116:117]
	v_pk_mul_f32 v[134:135], v[10:11], v[118:119]
	v_pk_mul_f32 v[136:137], v[12:13], v[120:121]
	v_pk_mul_f32 v[138:139], v[14:15], v[122:123]
	v_pk_mul_f32 v[140:141], v[16:17], v[124:125]
	v_pk_mul_f32 v[142:143], v[18:19], v[126:127]
	v_pk_mul_f32 v[144:145], v[20:21], v[128:129]
	v_pk_mul_f32 v[146:147], v[22:23], v[130:131]
	global_store_dwordx4 v2, v[132:135], s[34:35] offset:0 nt
	global_store_dwordx4 v2, v[136:139], s[34:35] offset:1024 nt
	global_store_dwordx4 v2, v[140:143], s[34:35] offset:2048 nt
	global_store_dwordx4 v2, v[144:147], s[34:35] offset:3072 nt
	s_waitcnt vmcnt(30)
	v_add_f32_dpp v112, v90, v90 quad_perm:[1,0,3,2] row_mask:0xf bank_mask:0xf
	s_mov_b64 s[36:37], s[24:25]
	s_add_u32 s24, s24, s22
	v_add_f32_dpp v112, v112, v112 quad_perm:[2,3,0,1] row_mask:0xf bank_mask:0xf
	s_addc_u32 s25, s25, 0
	s_nop 0
	v_add_f32_dpp v112, v112, v112 row_half_mirror row_mask:0xf bank_mask:0xf
	s_nop 1
	v_add_f32_dpp v112, v112, v112 row_mirror row_mask:0xf bank_mask:0xf
	v_fmamk_f32 v112, v112, 0x3a800000, v5
	v_rsq_f32_e32 v114, v112
	v_lshlrev_b32_e32 v116, 16, v82
	v_and_b32_e32 v117, 0xffff0000, v82
	v_lshlrev_b32_e32 v118, 16, v83
	v_and_b32_e32 v119, 0xffff0000, v83
	v_lshlrev_b32_e32 v120, 16, v84
	v_and_b32_e32 v121, 0xffff0000, v84
	v_lshlrev_b32_e32 v122, 16, v85
	v_and_b32_e32 v123, 0xffff0000, v85
	v_lshlrev_b32_e32 v124, 16, v86
	v_and_b32_e32 v125, 0xffff0000, v86
	v_lshlrev_b32_e32 v126, 16, v87
	v_and_b32_e32 v127, 0xffff0000, v87
	v_lshlrev_b32_e32 v128, 16, v88
	v_and_b32_e32 v129, 0xffff0000, v88
	v_lshlrev_b32_e32 v130, 16, v89
	v_and_b32_e32 v131, 0xffff0000, v89
	v_pk_mul_f32 v[116:117], v[114:115], v[116:117] op_sel_hi:[0,1]
	v_pk_mul_f32 v[118:119], v[114:115], v[118:119] op_sel_hi:[0,1]
	v_pk_mul_f32 v[120:121], v[114:115], v[120:121] op_sel_hi:[0,1]
	v_pk_mul_f32 v[122:123], v[114:115], v[122:123] op_sel_hi:[0,1]
	v_pk_mul_f32 v[124:125], v[114:115], v[124:125] op_sel_hi:[0,1]
	v_pk_mul_f32 v[126:127], v[114:115], v[126:127] op_sel_hi:[0,1]
	v_pk_mul_f32 v[128:129], v[114:115], v[128:129] op_sel_hi:[0,1]
	v_pk_mul_f32 v[130:131], v[114:115], v[130:131] op_sel_hi:[0,1]
	v_pk_mul_f32 v[132:133], v[8:9], v[116:117]
	v_pk_mul_f32 v[134:135], v[10:11], v[118:119]
	v_pk_mul_f32 v[136:137], v[12:13], v[120:121]
	v_pk_mul_f32 v[138:139], v[14:15], v[122:123]
	v_pk_mul_f32 v[140:141], v[16:17], v[124:125]
	v_pk_mul_f32 v[142:143], v[18:19], v[126:127]
	v_pk_mul_f32 v[144:145], v[20:21], v[128:129]
	v_pk_mul_f32 v[146:147], v[22:23], v[130:131]
	global_store_dwordx4 v2, v[132:135], s[36:37] offset:0 nt
	global_store_dwordx4 v2, v[136:139], s[36:37] offset:1024 nt
	global_store_dwordx4 v2, v[140:143], s[36:37] offset:2048 nt
	global_store_dwordx4 v2, v[144:147], s[36:37] offset:3072 nt
	s_waitcnt vmcnt(29)
	v_add_f32_dpp v112, v100, v100 quad_perm:[1,0,3,2] row_mask:0xf bank_mask:0xf
	s_mov_b64 s[34:35], s[24:25]
	s_add_u32 s24, s24, s22
	v_add_f32_dpp v112, v112, v112 quad_perm:[2,3,0,1] row_mask:0xf bank_mask:0xf
	s_addc_u32 s25, s25, 0
	s_nop 0
	v_add_f32_dpp v112, v112, v112 row_half_mirror row_mask:0xf bank_mask:0xf
	s_nop 1
	v_add_f32_dpp v112, v112, v112 row_mirror row_mask:0xf bank_mask:0xf
	v_fmamk_f32 v112, v112, 0x3a800000, v5
	v_rsq_f32_e32 v114, v112
	v_lshlrev_b32_e32 v116, 16, v92
	v_and_b32_e32 v117, 0xffff0000, v92
	v_lshlrev_b32_e32 v118, 16, v93
	v_and_b32_e32 v119, 0xffff0000, v93
	v_lshlrev_b32_e32 v120, 16, v94
	v_and_b32_e32 v121, 0xffff0000, v94
	v_lshlrev_b32_e32 v122, 16, v95
	v_and_b32_e32 v123, 0xffff0000, v95
	v_lshlrev_b32_e32 v124, 16, v96
	v_and_b32_e32 v125, 0xffff0000, v96
	v_lshlrev_b32_e32 v126, 16, v97
	v_and_b32_e32 v127, 0xffff0000, v97
	v_lshlrev_b32_e32 v128, 16, v98
	v_and_b32_e32 v129, 0xffff0000, v98
	v_lshlrev_b32_e32 v130, 16, v99
	v_and_b32_e32 v131, 0xffff0000, v99
	v_pk_mul_f32 v[116:117], v[114:115], v[116:117] op_sel_hi:[0,1]
	v_pk_mul_f32 v[118:119], v[114:115], v[118:119] op_sel_hi:[0,1]
	v_pk_mul_f32 v[120:121], v[114:115], v[120:121] op_sel_hi:[0,1]
	v_pk_mul_f32 v[122:123], v[114:115], v[122:123] op_sel_hi:[0,1]
	v_pk_mul_f32 v[124:125], v[114:115], v[124:125] op_sel_hi:[0,1]
	v_pk_mul_f32 v[126:127], v[114:115], v[126:127] op_sel_hi:[0,1]
	v_pk_mul_f32 v[128:129], v[114:115], v[128:129] op_sel_hi:[0,1]
	v_pk_mul_f32 v[130:131], v[114:115], v[130:131] op_sel_hi:[0,1]
	v_pk_mul_f32 v[132:133], v[8:9], v[116:117]
	v_pk_mul_f32 v[134:135], v[10:11], v[118:119]
	v_pk_mul_f32 v[136:137], v[12:13], v[120:121]
	v_pk_mul_f32 v[138:139], v[14:15], v[122:123]
	v_pk_mul_f32 v[140:141], v[16:17], v[124:125]
	v_pk_mul_f32 v[142:143], v[18:19], v[126:127]
	v_pk_mul_f32 v[144:145], v[20:21], v[128:129]
	v_pk_mul_f32 v[146:147], v[22:23], v[130:131]
	global_store_dwordx4 v2, v[132:135], s[34:35] offset:0 nt
	global_store_dwordx4 v2, v[136:139], s[34:35] offset:1024 nt
	global_store_dwordx4 v2, v[140:143], s[34:35] offset:2048 nt
	global_store_dwordx4 v2, v[144:147], s[34:35] offset:3072 nt
	s_waitcnt vmcnt(28)
	v_add_f32_dpp v112, v110, v110 quad_perm:[1,0,3,2] row_mask:0xf bank_mask:0xf
	s_mov_b64 s[36:37], s[24:25]
	s_add_u32 s24, s24, s22
	v_add_f32_dpp v112, v112, v112 quad_perm:[2,3,0,1] row_mask:0xf bank_mask:0xf
	s_addc_u32 s25, s25, 0
	s_nop 0
	v_add_f32_dpp v112, v112, v112 row_half_mirror row_mask:0xf bank_mask:0xf
	s_nop 1
	v_add_f32_dpp v112, v112, v112 row_mirror row_mask:0xf bank_mask:0xf
	v_fmamk_f32 v112, v112, 0x3a800000, v5
	v_rsq_f32_e32 v114, v112
	v_lshlrev_b32_e32 v116, 16, v102
	v_and_b32_e32 v117, 0xffff0000, v102
	v_lshlrev_b32_e32 v118, 16, v103
	v_and_b32_e32 v119, 0xffff0000, v103
	v_lshlrev_b32_e32 v120, 16, v104
	v_and_b32_e32 v121, 0xffff0000, v104
	v_lshlrev_b32_e32 v122, 16, v105
	v_and_b32_e32 v123, 0xffff0000, v105
	v_lshlrev_b32_e32 v124, 16, v106
	v_and_b32_e32 v125, 0xffff0000, v106
	v_lshlrev_b32_e32 v126, 16, v107
	v_and_b32_e32 v127, 0xffff0000, v107
	v_lshlrev_b32_e32 v128, 16, v108
	v_and_b32_e32 v129, 0xffff0000, v108
	v_lshlrev_b32_e32 v130, 16, v109
	v_and_b32_e32 v131, 0xffff0000, v109
	v_pk_mul_f32 v[116:117], v[114:115], v[116:117] op_sel_hi:[0,1]
	v_pk_mul_f32 v[118:119], v[114:115], v[118:119] op_sel_hi:[0,1]
	v_pk_mul_f32 v[120:121], v[114:115], v[120:121] op_sel_hi:[0,1]
	v_pk_mul_f32 v[122:123], v[114:115], v[122:123] op_sel_hi:[0,1]
	v_pk_mul_f32 v[124:125], v[114:115], v[124:125] op_sel_hi:[0,1]
	v_pk_mul_f32 v[126:127], v[114:115], v[126:127] op_sel_hi:[0,1]
	v_pk_mul_f32 v[128:129], v[114:115], v[128:129] op_sel_hi:[0,1]
	v_pk_mul_f32 v[130:131], v[114:115], v[130:131] op_sel_hi:[0,1]
	v_pk_mul_f32 v[132:133], v[8:9], v[116:117]
	v_pk_mul_f32 v[134:135], v[10:11], v[118:119]
	v_pk_mul_f32 v[136:137], v[12:13], v[120:121]
	v_pk_mul_f32 v[138:139], v[14:15], v[122:123]
	v_pk_mul_f32 v[140:141], v[16:17], v[124:125]
	v_pk_mul_f32 v[142:143], v[18:19], v[126:127]
	v_pk_mul_f32 v[144:145], v[20:21], v[128:129]
	v_pk_mul_f32 v[146:147], v[22:23], v[130:131]
	global_store_dwordx4 v2, v[132:135], s[36:37] offset:0 nt
	global_store_dwordx4 v2, v[136:139], s[36:37] offset:1024 nt
	global_store_dwordx4 v2, v[140:143], s[36:37] offset:2048 nt
	global_store_dwordx4 v2, v[144:147], s[36:37] offset:3072 nt
.Lfin_tail:
	s_cmp_lt_i32 s12, 0x10000
	s_cbranch_scc0 .LBB0_3641
	s_mov_b64 s[26:27], s[16:17]
	s_mov_b64 s[28:29], s[18:19]
	global_load_dword v40, v4, s[26:27]
	global_load_dwordx2 v[32:33], v3, s[28:29] offset:0
	global_load_dwordx2 v[34:35], v3, s[28:29] offset:512
	global_load_dwordx2 v[36:37], v3, s[28:29] offset:1024
	global_load_dwordx2 v[38:39], v3, s[28:29] offset:1536
	s_add_u32 s16, s16, s20
	s_addc_u32 s17, s17, 0
	s_add_u32 s18, s18, s21
	s_addc_u32 s19, s19, 0
	s_add_i32 s12, s12, s13
	s_waitcnt vmcnt(0)
	v_add_f32_dpp v112, v40, v40 quad_perm:[1,0,3,2] row_mask:0xf bank_mask:0xf
	s_mov_b64 s[34:35], s[24:25]
	s_add_u32 s24, s24, s22
	v_add_f32_dpp v112, v112, v112 quad_perm:[2,3,0,1] row_mask:0xf bank_mask:0xf
	s_addc_u32 s25, s25, 0
	s_nop 0
	v_add_f32_dpp v112, v112, v112 row_half_mirror row_mask:0xf bank_mask:0xf
	s_nop 1
	v_add_f32_dpp v112, v112, v112 row_mirror row_mask:0xf bank_mask:0xf
	v_fmamk_f32 v112, v112, 0x3a800000, v5
	v_rsq_f32_e32 v114, v112
	v_lshlrev_b32_e32 v116, 16, v32
	v_and_b32_e32 v117, 0xffff0000, v32
	v_lshlrev_b32_e32 v118, 16, v33
	v_and_b32_e32 v119, 0xffff0000, v33
	v_lshlrev_b32_e32 v120, 16, v34
	v_and_b32_e32 v121, 0xffff0000, v34
	v_lshlrev_b32_e32 v122, 16, v35
	v_and_b32_e32 v123, 0xffff0000, v35
	v_lshlrev_b32_e32 v124, 16, v36
	v_and_b32_e32 v125, 0xffff0000, v36
	v_lshlrev_b32_e32 v126, 16, v37
	v_and_b32_e32 v127, 0xffff0000, v37
	v_lshlrev_b32_e32 v128, 16, v38
	v_and_b32_e32 v129, 0xffff0000, v38
	v_lshlrev_b32_e32 v130, 16, v39
	v_and_b32_e32 v131, 0xffff0000, v39
	v_pk_mul_f32 v[116:117], v[114:115], v[116:117] op_sel_hi:[0,1]
	v_pk_mul_f32 v[118:119], v[114:115], v[118:119] op_sel_hi:[0,1]
	v_pk_mul_f32 v[120:121], v[114:115], v[120:121] op_sel_hi:[0,1]
	v_pk_mul_f32 v[122:123], v[114:115], v[122:123] op_sel_hi:[0,1]
	v_pk_mul_f32 v[124:125], v[114:115], v[124:125] op_sel_hi:[0,1]
	v_pk_mul_f32 v[126:127], v[114:115], v[126:127] op_sel_hi:[0,1]
	v_pk_mul_f32 v[128:129], v[114:115], v[128:129] op_sel_hi:[0,1]
	v_pk_mul_f32 v[130:131], v[114:115], v[130:131] op_sel_hi:[0,1]
	v_pk_mul_f32 v[132:133], v[8:9], v[116:117]
	v_pk_mul_f32 v[134:135], v[10:11], v[118:119]
	v_pk_mul_f32 v[136:137], v[12:13], v[120:121]
	v_pk_mul_f32 v[138:139], v[14:15], v[122:123]
	v_pk_mul_f32 v[140:141], v[16:17], v[124:125]
	v_pk_mul_f32 v[142:143], v[18:19], v[126:127]
	v_pk_mul_f32 v[144:145], v[20:21], v[128:129]
	v_pk_mul_f32 v[146:147], v[22:23], v[130:131]
	global_store_dwordx4 v2, v[132:135], s[34:35] offset:0 nt
	global_store_dwordx4 v2, v[136:139], s[34:35] offset:1024 nt
	global_store_dwordx4 v2, v[140:143], s[34:35] offset:2048 nt
	global_store_dwordx4 v2, v[144:147], s[34:35] offset:3072 nt
	s_branch .Lfin_tail
